# split grid barrier in front of norm_kvq: weight-table build (kernel inputs only) before the wait, K/V padding zero-fill moved behind it; on top of v71
# speedup vs baseline: 1.0070x; 1.0015x over previous
.Lcv_skip:
	s_cmp_gt_i32 s81, 7
	s_cselect_b64 s[4:5], -1, 0
	s_and_b64 s[0:1], s[76:77], s[4:5]
	v_readlane_b32 s86, v253, 40
	s_andn2_b64 vcc, exec, s[0:1]
	v_readlane_b32 s76, v253, 62
	v_readlane_b32 s77, v253, 63
	v_readlane_b32 s87, v253, 41
	s_cbranch_vccnz .LBB0_1205
	s_waitcnt vmcnt(0)
	s_waitcnt vmcnt(0) lgkmcnt(0)
	s_barrier
	s_and_saveexec_b64 s[0:1], s[78:79]
	s_cbranch_execz .LBB0_1204
	v_mov_b32_e32 v1, 0x22160
	s_waitcnt vmcnt(0) lgkmcnt(0)
	ds_read_b32 v2, v1
	v_mov_b32_e32 v3, 1
	v_mov_b32_e32 v4, s99
	v_and_b32_e32 v5, 0xffff, v4
	v_lshrrev_b32_e32 v6, 16, v4
	global_atomic_add v7, v5, v3, s[100:101] sc0
	buffer_inv sc1
	v_lshrrev_b32_e32 v8, 8, v5
	v_sub_u32_e32 v8, s98, v8
	v_add_u32_e32 v8, 7, v8
	v_lshrrev_b32_e32 v8, 3, v8
	v_mov_b32_e32 v9, s98
	v_min_u32_e32 v9, 8, v9
	v_mov_b32_e32 v10, 0
	s_waitcnt lgkmcnt(0)
	v_add_u32_e32 v2, 1, v2
	ds_write_b32 v1, v2
	v_mul_lo_u32 v8, v8, v2
	v_mul_lo_u32 v9, v9, v2
	s_waitcnt vmcnt(0)
	v_add_u32_e32 v7, 1, v7
	v_cmp_eq_u32_e32 vcc, v7, v8
	s_cbranch_vccz .Lgb_done_7
	v_mov_b32_e32 v4, 0
	global_atomic_add v4, v3, s[100:101] offset:2048
	global_atomic_add v4, v3, s[100:101] offset:2304
	global_atomic_add v4, v3, s[100:101] offset:2560
	global_atomic_add v4, v3, s[100:101] offset:2816
	global_atomic_add v4, v3, s[100:101] offset:3072
	global_atomic_add v4, v3, s[100:101] offset:3328
	global_atomic_add v4, v3, s[100:101] offset:3584
	global_atomic_add v4, v3, s[100:101] offset:3840
.Lgb_done_7:
	s_waitcnt lgkmcnt(0)
.LBB0_1204:
	s_or_b64 exec, exec, s[0:1]
	s_waitcnt lgkmcnt(0)
.LBB0_1205:
	s_cmp_lt_i32 s80, 8
	s_cselect_b64 s[6:7], -1, 0
	s_add_u32 s0, s54, 0x1300000
	s_addc_u32 s1, s55, 0
	s_add_u32 s10, s54, 0x1600000
	s_addc_u32 s11, s55, 0
	s_add_u32 s58, s54, 0x7d00000
	s_addc_u32 s59, s55, 0
	s_and_b64 s[12:13], s[6:7], s[4:5]
	s_andn2_b64 vcc, exec, s[12:13]
	s_cbranch_vccnz .LBB0_1220
.LBB0_1209:
	v_readlane_b32 s60, v253, 18
	v_lshlrev_b32_e32 v2, 2, v0
	v_mov_b32_e32 v3, 0
	v_readlane_b32 s61, v253, 19
	v_readlane_b32 s62, v253, 20
	v_readlane_b32 s63, v253, 21
	s_waitcnt vmcnt(0)
	v_lshl_add_u64 v[6:7], s[60:61], 0, v[2:3]
	s_movk_i32 s4, 0x2040
	v_mov_b64_e32 v[2:3], s[62:63]
	v_mad_u64_u32 v[2:3], s[4:5], v0, s4, v[2:3]
	s_mov_b64 s[4:5], 0x2000
	v_or_b32_e32 v1, 0xfffffe00, v0
	v_lshl_add_u32 v10, v0, 1, 0
	v_lshl_add_u64 v[8:9], v[2:3], 0, s[4:5]
	s_mov_b64 s[4:5], 0
	s_movk_i32 s14, 0x7fff
	s_mov_b64 s[6:7], 0x800
	s_mov_b64 s[8:9], 0x408000
	v_readlane_b32 s64, v253, 22
	v_readlane_b32 s65, v253, 23
	v_readlane_b32 s66, v253, 24
	v_readlane_b32 s67, v253, 25
	v_readlane_b32 s68, v253, 26
	v_readlane_b32 s69, v253, 27
	v_readlane_b32 s70, v253, 28
	v_readlane_b32 s71, v253, 29
	v_readlane_b32 s72, v253, 30
	v_readlane_b32 s73, v253, 31
	v_readlane_b32 s74, v253, 32
	v_readlane_b32 s75, v253, 33
.LBB0_1210:
	global_load_dword v11, v[6:7], off
	global_load_dwordx4 v[12:15], v[8:9], off
	global_load_dwordx4 v[16:19], v[8:9], off offset:16
	global_load_dwordx4 v[20:23], v[8:9], off offset:32
	global_load_dwordx4 v[2:5], v[8:9], off offset:48
	v_add_co_u32_e32 v1, vcc, 0x200, v1
	s_xor_b64 s[16:17], vcc, -1
	s_and_b64 s[16:17], exec, s[16:17]
	v_lshl_add_u64 v[6:7], v[6:7], 0, s[6:7]
	v_lshl_add_u64 v[8:9], v[8:9], 0, s[8:9]
	s_or_b64 s[4:5], s[16:17], s[4:5]
	s_waitcnt vmcnt(0)
	v_mul_f32_e32 v24, v11, v12
	v_mul_f32_e32 v25, v11, v13
	v_mul_f32_e32 v26, v11, v14
	v_mul_f32_e32 v27, v11, v15
	v_mul_f32_e32 v28, v11, v16
	v_mul_f32_e32 v29, v11, v17
	v_mul_f32_e32 v30, v11, v18
	v_mul_f32_e32 v31, v11, v19
	v_mul_f32_e32 v32, v11, v20
	v_mul_f32_e32 v33, v11, v21
	v_mul_f32_e32 v34, v11, v22
	v_mul_f32_e32 v35, v11, v23
	v_mul_f32_e32 v36, v11, v2
	v_mul_f32_e32 v37, v11, v3
	v_mul_f32_e32 v38, v11, v4
	v_mul_f32_e32 v39, v11, v5
	v_bfe_u32 v40, v24, 16, 1
	v_bfe_u32 v41, v25, 16, 1
	v_bfe_u32 v42, v26, 16, 1
	v_bfe_u32 v43, v27, 16, 1
	v_bfe_u32 v44, v28, 16, 1
	v_bfe_u32 v45, v29, 16, 1
	v_bfe_u32 v46, v30, 16, 1
	v_bfe_u32 v47, v31, 16, 1
	v_bfe_u32 v48, v32, 16, 1
	v_bfe_u32 v49, v33, 16, 1
	v_bfe_u32 v50, v34, 16, 1
	v_bfe_u32 v51, v35, 16, 1
	v_bfe_u32 v52, v36, 16, 1
	v_bfe_u32 v53, v37, 16, 1
	v_bfe_u32 v54, v38, 16, 1
	v_bfe_u32 v55, v39, 16, 1
	v_add3_u32 v24, v24, v40, s14
	v_add3_u32 v25, v25, v41, s14
	v_add3_u32 v26, v26, v42, s14
	v_add3_u32 v27, v27, v43, s14
	v_add3_u32 v28, v28, v44, s14
	v_add3_u32 v29, v29, v45, s14
	v_add3_u32 v30, v30, v46, s14
	v_add3_u32 v31, v31, v47, s14
	v_add3_u32 v32, v32, v48, s14
	v_add3_u32 v33, v33, v49, s14
	v_add3_u32 v34, v34, v50, s14
	v_add3_u32 v35, v35, v51, s14
	v_add3_u32 v36, v36, v52, s14
	v_add3_u32 v37, v37, v53, s14
	v_add3_u32 v38, v38, v54, s14
	v_add3_u32 v39, v39, v55, s14
	ds_write_b16_d16_hi v10, v24
	v_and_b32_e32 v24, 0xffff0000, v24
	ds_write_b16_d16_hi v10, v25 offset:2048
	v_and_b32_e32 v25, 0xffff0000, v25
	ds_write_b16_d16_hi v10, v26 offset:4096
	v_and_b32_e32 v26, 0xffff0000, v26
	ds_write_b16_d16_hi v10, v27 offset:6144
	v_and_b32_e32 v27, 0xffff0000, v27
	ds_write_b16_d16_hi v10, v28 offset:8192
	v_and_b32_e32 v28, 0xffff0000, v28
	ds_write_b16_d16_hi v10, v29 offset:10240
	v_and_b32_e32 v29, 0xffff0000, v29
	ds_write_b16_d16_hi v10, v30 offset:12288
	v_and_b32_e32 v30, 0xffff0000, v30
	ds_write_b16_d16_hi v10, v31 offset:14336
	v_and_b32_e32 v31, 0xffff0000, v31
	ds_write_b16_d16_hi v10, v32 offset:16384
	v_and_b32_e32 v32, 0xffff0000, v32
	ds_write_b16_d16_hi v10, v33 offset:18432
	v_and_b32_e32 v33, 0xffff0000, v33
	ds_write_b16_d16_hi v10, v34 offset:20480
	v_and_b32_e32 v34, 0xffff0000, v34
	ds_write_b16_d16_hi v10, v35 offset:22528
	v_and_b32_e32 v35, 0xffff0000, v35
	ds_write_b16_d16_hi v10, v36 offset:24576
	v_and_b32_e32 v36, 0xffff0000, v36
	ds_write_b16_d16_hi v10, v37 offset:26624
	v_and_b32_e32 v37, 0xffff0000, v37
	ds_write_b16_d16_hi v10, v38 offset:28672
	v_and_b32_e32 v38, 0xffff0000, v38
	ds_write_b16_d16_hi v10, v39 offset:30720
	v_and_b32_e32 v39, 0xffff0000, v39
	v_fma_f32 v12, v11, v12, -v24
	v_fma_f32 v13, v11, v13, -v25
	v_fma_f32 v14, v11, v14, -v26
	v_fma_f32 v15, v11, v15, -v27
	v_fma_f32 v16, v11, v16, -v28
	v_fma_f32 v17, v11, v17, -v29
	v_fma_f32 v18, v11, v18, -v30
	v_fma_f32 v19, v11, v19, -v31
	v_fma_f32 v20, v11, v20, -v32
	v_fma_f32 v21, v11, v21, -v33
	v_fma_f32 v22, v11, v22, -v34
	v_fma_f32 v23, v11, v23, -v35
	v_fma_f32 v2, v11, v2, -v36
	v_fma_f32 v3, v11, v3, -v37
	v_fma_f32 v4, v11, v4, -v38
	v_fma_f32 v5, v11, v5, -v39
	v_bfe_u32 v11, v12, 16, 1
	v_bfe_u32 v24, v13, 16, 1
	v_bfe_u32 v25, v14, 16, 1
	v_bfe_u32 v26, v15, 16, 1
	v_bfe_u32 v27, v16, 16, 1
	v_bfe_u32 v28, v17, 16, 1
	v_bfe_u32 v29, v18, 16, 1
	v_bfe_u32 v30, v19, 16, 1
	v_bfe_u32 v31, v20, 16, 1
	v_bfe_u32 v32, v21, 16, 1
	v_bfe_u32 v33, v22, 16, 1
	v_bfe_u32 v34, v23, 16, 1
	v_bfe_u32 v35, v2, 16, 1
	v_bfe_u32 v36, v3, 16, 1
	v_bfe_u32 v37, v4, 16, 1
	v_bfe_u32 v38, v5, 16, 1
	v_add3_u32 v11, v12, v11, s14
	v_add3_u32 v12, v13, v24, s14
	v_add3_u32 v13, v14, v25, s14
	v_add3_u32 v14, v15, v26, s14
	v_add3_u32 v15, v16, v27, s14
	v_add3_u32 v16, v17, v28, s14
	v_add3_u32 v17, v18, v29, s14
	v_add3_u32 v18, v19, v30, s14
	v_add3_u32 v19, v20, v31, s14
	v_add3_u32 v20, v21, v32, s14
	v_add3_u32 v21, v22, v33, s14
	v_add3_u32 v22, v23, v34, s14
	v_add3_u32 v2, v2, v35, s14
	v_add3_u32 v3, v3, v36, s14
	v_add3_u32 v4, v4, v37, s14
	v_add3_u32 v5, v5, v38, s14
	ds_write_b16_d16_hi v10, v11 offset:32768
	ds_write_b16_d16_hi v10, v12 offset:34816
	ds_write_b16_d16_hi v10, v13 offset:36864
	ds_write_b16_d16_hi v10, v14 offset:38912
	ds_write_b16_d16_hi v10, v15 offset:40960
	ds_write_b16_d16_hi v10, v16 offset:43008
	ds_write_b16_d16_hi v10, v17 offset:45056
	ds_write_b16_d16_hi v10, v18 offset:47104
	ds_write_b16_d16_hi v10, v19 offset:49152
	ds_write_b16_d16_hi v10, v20 offset:51200
	ds_write_b16_d16_hi v10, v21 offset:53248
	ds_write_b16_d16_hi v10, v22 offset:55296
	ds_write_b16_d16_hi v10, v2 offset:57344
	ds_write_b16_d16_hi v10, v3 offset:59392
	ds_write_b16_d16_hi v10, v4 offset:61440
	ds_write_b16_d16_hi v10, v5 offset:63488
	v_add_u32_e32 v10, 0x400, v10
	s_andn2_b64 exec, exec, s[4:5]
	s_cbranch_execnz .LBB0_1210
	s_or_b64 exec, exec, s[4:5]
	s_and_saveexec_b64 s[4:5], s[78:79]
	s_cbranch_execz .Lgw_end_7
	v_mov_b32_e32 v1, 0x22160
	ds_read_b32 v2, v1
	v_mov_b32_e32 v3, s99
	v_lshrrev_b32_e32 v4, 16, v3
	v_mov_b32_e32 v5, s98
	v_min_u32_e32 v5, 8, v5
	v_mov_b32_e32 v6, 0
	s_waitcnt lgkmcnt(0)
	v_mul_lo_u32 v5, v5, v2

.Lgw_end_7:
	s_or_b64 exec, exec, s[4:5]
	s_barrier
	s_cmpk_lt_i32 s93, 0xc0
	s_cbranch_scc0 .Lp7_after_fill
	s_bitcmp0_b32 s77, 6
	s_mov_b32 s4, 0
	s_cselect_b32 s7, s27, s59
	s_cselect_b32 s6, s26, s58
	v_lshlrev_b32_e32 v2, 5, v208
	v_mov_b32_e32 v3, 0
	s_mov_b32 s5, s4
	v_lshl_add_u64 v[2:3], s[6:7], 0, v[2:3]
	s_mov_b32 s6, s4
	s_mov_b32 s7, s4
	s_waitcnt vmcnt(0)
	v_mov_b64_e32 v[4:5], s[4:5]
	v_mov_b64_e32 v[6:7], s[6:7]

.Lp7_after_fill:
	s_lshl_b32 s16, s95, 6
	v_or_b32_e32 v2, s16, v222
	v_ashrrev_i32_e32 v3, 31, v2
	v_lshlrev_b64 v[2:3], 11, v[2:3]
	v_and_b32_e32 v4, 48, v0
	v_bfe_u32 v20, v0, 2, 4
	v_readlane_b32 s60, v253, 18
	v_lshl_add_u64 v[2:3], s[2:3], 0, v[2:3]
	v_lshl_or_b32 v18, s92, 8, v4
	v_mov_b32_e32 v19, 0
	v_lshlrev_b32_e32 v1, 2, v20
	v_readlane_b32 s64, v253, 22
	v_readlane_b32 s65, v253, 23
	v_lshl_add_u64 v[14:15], v[2:3], 0, v[18:19]
	s_waitcnt lgkmcnt(0)
	s_barrier
	v_lshl_add_u64 v[34:35], s[2:3], 0, v[18:19]
	s_nop 0
	global_load_dword v1, v1, s[64:65]
	s_nop 0
	global_load_dwordx4 v[2:5], v[14:15], off
	global_load_dwordx4 v[6:9], v[14:15], off offset:64
	global_load_dwordx4 v[10:13], v[14:15], off offset:128
	s_nop 0
	global_load_dwordx4 v[14:17], v[14:15], off offset:192
	v_mbcnt_hi_u32_b32 v19, -1, v227
	v_and_b32_e32 v22, 64, v19
	v_xor_b32_e32 v21, 16, v19
	v_add_u32_e32 v22, 64, v22
	v_cmp_lt_i32_e32 vcc, v21, v22
	s_cmp_eq_u32 s95, 0
	v_and_b32_e32 v44, 3, v0
	v_cndmask_b32_e32 v21, v19, v21, vcc
	v_lshlrev_b32_e32 v40, 2, v21
	v_xor_b32_e32 v21, 32, v19
	v_cmp_lt_i32_e32 vcc, v21, v22
	s_cselect_b32 s18, 5, 4
	s_and_b32 s4, s77, 0xffffffc0
	v_cndmask_b32_e32 v19, v19, v21, vcc
	v_lshlrev_b32_e32 v41, 2, v19
	v_lshlrev_b32_e32 v19, 11, v222
	s_add_i32 s6, 0, 0x10000
	v_and_or_b32 v45, v226, 12, v44
	v_add3_u32 v42, 0, v19, v18
	s_add_i32 s4, s6, s4
	v_lshl_add_u32 v46, v45, 2, s6
	s_mov_b32 s6, 0x10400
	v_mov_b64_e32 v[18:19], s[10:11]
	v_lshl_add_u32 v43, v208, 2, s4
	s_movk_i32 s4, 0x100
	v_and_b32_e32 v21, 0xfc, v0
	v_mad_u64_u32 v[36:37], s[6:7], v20, s6, v[18:19]
	s_mov_b32 s17, 0
	v_cmp_gt_u32_e32 vcc, 16, v208
	s_lshl_b32 s19, s92, 10
	v_cmp_gt_u32_e64 s[4:5], s4, v0
	v_cmp_eq_u32_e64 s[6:7], 0, v20
	v_lshlrev_b32_e32 v47, 2, v21
	v_mov_b32_e32 v48, 0x358637bd
	s_mov_b32 s20, 0x800000
	s_mov_b32 s21, 0xbfb8aa3b
	s_mov_b32 s22, 0xb2a5705f
	s_mov_b32 s23, 0x42ce8ed0
	s_mov_b32 s30, 0xc2b17218
	s_mov_b32 s31, 0x7f800000
	s_mov_b32 s34, 0x3f2aaaab
	v_mov_b32_e32 v49, 0x3ecc95a3
	s_mov_b32 s35, 0x3f317218
	s_mov_b32 s36, 0x33800000
	v_mov_b32_e32 v50, 0x7f800000
	v_mov_b32_e32 v38, 0x3f317218
	v_readlane_b32 s61, v253, 19
	v_readlane_b32 s62, v253, 20
	v_readlane_b32 s63, v253, 21
	v_readlane_b32 s66, v253, 24
	v_readlane_b32 s67, v253, 25
	v_readlane_b32 s68, v253, 26
	v_readlane_b32 s69, v253, 27
	v_readlane_b32 s70, v253, 28
	v_readlane_b32 s71, v253, 29
	v_readlane_b32 s72, v253, 30
	v_readlane_b32 s73, v253, 31
	v_readlane_b32 s74, v253, 32
	v_readlane_b32 s75, v253, 33
	s_branch .LBB0_1213
